# speedup vs baseline: 1.1105x; 1.0105x over previous
.LBB0_15:
	s_or_b64 exec, exec, s[6:7]
	v_lshlrev_b32_e32 v26, 1, v0
	s_movk_i32 s3, 0xc4
	v_cmp_gt_u32_e64 s[6:7], s3, v0
	v_lshlrev_b32_e32 v13, 2, v26
	s_barrier
	s_and_saveexec_b64 s[8:9], s[6:7]
	ds_read_b32 v27, v13 offset:15648
	s_or_b64 exec, exec, s[8:9]
	s_movk_i32 s3, 0x100
	v_cmp_gt_u32_e64 s[10:11], s3, v0
	v_or_b32_e32 v26, 1, v26
	s_movk_i32 s3, 0x187
	v_cmp_gt_u32_e64 s[8:9], s3, v26
	s_and_b64 s[36:37], s[10:11], s[8:9]
	v_mov_b32_e32 v26, 0
	s_and_saveexec_b64 s[12:13], s[36:37]
	ds_read_b32 v26, v13 offset:15652
	s_or_b64 exec, exec, s[12:13]
	s_waitcnt lgkmcnt(0)
	v_add_u32_e32 v28, v26, v27
	v_and_b32_e32 v35, 0x33f, v0
	v_cmp_eq_u32_e64 s[24:25], 63, v35
	v_mov_b32_e32 v29, v28
	s_nop 1
	v_add_u32_dpp v29, v28, v28 row_shr:1 row_mask:0xf bank_mask:0xf bound_ctrl:0
	v_add_u32_dpp v29, v28, v29 row_shr:2 row_mask:0xf bank_mask:0xf bound_ctrl:0
	v_add_u32_dpp v29, v28, v29 row_shr:3 row_mask:0xf bank_mask:0xf bound_ctrl:0
	s_nop 1
	v_add_u32_dpp v29, v29, v29 row_shr:4 row_mask:0xf bank_mask:0xe
	s_nop 1
	v_add_u32_dpp v29, v29, v29 row_shr:8 row_mask:0xf bank_mask:0xc
	s_nop 1
	v_add_u32_dpp v29, v29, v29 row_bcast:15 row_mask:0xa bank_mask:0xf
	s_nop 1
	v_add_u32_dpp v29, v29, v29 row_bcast:31 row_mask:0xc bank_mask:0xf
	s_nop 1
	v_lshrrev_b32_e32 v26, 6, v0
	v_lshlrev_b32_e32 v35, 2, v26
	s_and_saveexec_b64 s[28:29], s[24:25]
	ds_write_b32 v35, v29 offset:18784
	s_or_b64 exec, exec, s[28:29]
	s_load_dwordx2 s[34:35], s[0:1], 0x10
	s_waitcnt lgkmcnt(0)
	s_barrier
	s_and_saveexec_b64 s[30:31], s[10:11]
	s_cbranch_execz .LBB0_30
	v_mov_b32_e32 v37, 0
	s_and_saveexec_b64 s[38:39], s[26:27]
	s_cbranch_execz .LBB0_26
	s_movk_i32 s3, 0x4960
	s_mov_b64 s[40:41], 0
	v_mov_b32_e32 v37, 0
	v_mov_b32_e32 v38, v26

.LBB0_30:
	s_or_b64 exec, exec, s[30:31]
	s_load_dwordx4 s[28:31], s[0:1], 0x18
	s_load_dwordx2 s[38:39], s[0:1], 0x28
	v_add_u32_e32 v29, 0x3d20, v14
	v_add_u32_e32 v28, 0x4340, v16
	v_lshl_or_b32 v16, v17, 16, v15
	v_add_u32_e32 v27, 0x3d20, v19
	v_add_u32_e32 v19, 0x4340, v20
	v_lshl_or_b32 v15, v21, 16, v18
	v_add_u32_e32 v18, 0x3d20, v23
	v_add_u32_e32 v17, 0x4340, v24
	v_lshl_or_b32 v14, v25, 16, v22
	v_mov_b32_e32 v21, 0
	v_mov_b32_e32 v20, 0
	s_waitcnt lgkmcnt(0)
	s_barrier
	s_and_saveexec_b64 s[40:41], s[6:7]
	ds_read_b32 v20, v13 offset:17216
	s_or_b64 exec, exec, s[40:41]
	s_and_saveexec_b64 s[40:41], s[36:37]
	ds_read_b32 v21, v13 offset:17220
	s_or_b64 exec, exec, s[40:41]
	s_waitcnt lgkmcnt(0)
	v_add_u32_e32 v21, v21, v20
	v_mov_b32_e32 v22, v21
	s_nop 1
	v_add_u32_dpp v22, v21, v21 row_shr:1 row_mask:0xf bank_mask:0xf bound_ctrl:0
	v_add_u32_dpp v22, v21, v22 row_shr:2 row_mask:0xf bank_mask:0xf bound_ctrl:0
	v_add_u32_dpp v22, v21, v22 row_shr:3 row_mask:0xf bank_mask:0xf bound_ctrl:0
	s_nop 1
	v_add_u32_dpp v22, v22, v22 row_shr:4 row_mask:0xf bank_mask:0xe
	s_nop 1
	v_add_u32_dpp v22, v22, v22 row_shr:8 row_mask:0xf bank_mask:0xc
	s_nop 1
	v_add_u32_dpp v22, v22, v22 row_bcast:15 row_mask:0xa bank_mask:0xf
	s_nop 1
	v_add_u32_dpp v22, v22, v22 row_bcast:31 row_mask:0xc bank_mask:0xf
	s_nop 1
	s_and_saveexec_b64 s[12:13], s[24:25]
	ds_write_b32 v35, v22 offset:18784
	s_or_b64 exec, exec, s[12:13]
	s_waitcnt lgkmcnt(0)
	s_barrier
	s_and_saveexec_b64 s[12:13], s[10:11]
	s_cbranch_execz .LBB0_45
	v_mov_b32_e32 v23, 0
	s_and_saveexec_b64 s[14:15], s[26:27]
	s_cbranch_execz .LBB0_41
	s_movk_i32 s3, 0x4960
	s_mov_b64 s[16:17], 0
	v_mov_b32_e32 v23, 0

.LBB2_8:
	s_or_b64 exec, exec, s[4:5]
	v_mov_b32_e32 v12, 0
	s_waitcnt lgkmcnt(0)
	s_barrier
	ds_read_b128 v[2:5], v12 offset:4096
	v_lshlrev_b32_e32 v7, 1, v0
	v_cmp_lt_u32_e64 s[4:5], 63, v0
	v_cmp_gt_u32_e64 s[0:1], 64, v0
	v_lshlrev_b32_e32 v7, 2, v7
	v_mov_b32_e32 v9, 0
	s_and_saveexec_b64 s[8:9], s[0:1]
	ds_read_b32 v9, v7 offset:3328
	s_or_b64 exec, exec, s[8:9]
	s_and_saveexec_b64 s[8:9], s[0:1]
	ds_read_b32 v12, v7 offset:3332
	s_or_b64 exec, exec, s[8:9]
	s_waitcnt lgkmcnt(0)
	v_add_u32_e32 v12, v12, v9
	v_mov_b32_e32 v10, v12
	s_nop 1
	v_add_u32_dpp v10, v12, v12 row_shr:1 row_mask:0xf bank_mask:0xf bound_ctrl:0
	v_add_u32_dpp v10, v12, v10 row_shr:2 row_mask:0xf bank_mask:0xf bound_ctrl:0
	v_add_u32_dpp v10, v12, v10 row_shr:3 row_mask:0xf bank_mask:0xf bound_ctrl:0
	s_nop 1
	v_add_u32_dpp v10, v10, v10 row_shr:4 row_mask:0xf bank_mask:0xe
	s_nop 1
	v_add_u32_dpp v10, v10, v10 row_shr:8 row_mask:0xf bank_mask:0xc
	s_nop 1
	v_add_u32_dpp v10, v10, v10 row_bcast:15 row_mask:0xa bank_mask:0xf
	s_nop 1
	v_add_u32_dpp v10, v10, v10 row_bcast:31 row_mask:0xc bank_mask:0xf
	s_nop 1
	v_cmp_eq_u32_e64 s[6:7], 63, v24
	s_and_saveexec_b64 s[8:9], s[6:7]
	ds_write_b32 v13, v10 offset:4112
	s_or_b64 exec, exec, s[8:9]
	v_mov_b32_e32 v11, 0
	s_waitcnt lgkmcnt(0)
	s_barrier
	s_and_saveexec_b64 s[6:7], s[4:5]
	s_cbranch_execz .LBB2_24
	v_add_u32_e32 v11, -1, v8
	v_cmp_lt_u32_e64 s[4:5], 6, v11
	v_mov_b32_e32 v11, 0
	s_and_saveexec_b64 s[8:9], s[4:5]
	s_cbranch_execz .LBB2_19
	s_mov_b32 s3, 0
	s_movk_i32 s10, 0x1010
	s_mov_b64 s[4:5], 0
	v_mov_b32_e32 v11, 0

_Z6k_mainPKiPKjPK15HIP_vector_typeIfLj2EEPKfS8_PKDF16_S8_Pf:
	s_mul_hi_i32 s3, s2, 0xc350
	s_mul_i32 s6, s2, 0xc350
	s_lshr_b32 s4, s3, 24
	s_add_u32 s4, s6, s4
	s_addc_u32 s5, s3, 0
	s_add_i32 s3, s2, 1
	s_mul_hi_i32 s3, s3, 0xc350
	s_lshr_b64 s[24:25], s[4:5], 8
	s_add_i32 s6, s6, 0xc350
	s_lshr_b32 s4, s3, 24
	s_add_u32 s4, s6, s4
	s_addc_u32 s5, s3, 0
	s_lshr_b64 s[4:5], s[4:5], 8
	s_sub_i32 s3, s4, s24
	s_load_dwordx2 s[34:35], s[0:1], 0x0
	s_load_dwordx2 s[18:19], s[0:1], 0x8
	s_load_dwordx4 s[44:47], s[0:1], 0x18
	s_lshl_b32 s36, s24, 2
	s_add_i32 s37, s24, s3
	s_lshl_b32 s37, s37, 2
	s_lshl_b32 s30, s3, 2
	v_cmp_ge_i32_e64 s[40:41], s3, v0
	s_waitcnt lgkmcnt(0)
	s_load_dword s38, s[34:35], s36
	s_load_dword s39, s[34:35], s37
	s_and_saveexec_b64 s[42:43], s[40:41]
	s_cbranch_execz .Lrp_skip
	v_add_u32_e32 v2, s24, v0
	v_ashrrev_i32_e32 v3, 31, v2
	v_lshl_add_u64 v[2:3], v[2:3], 2, s[34:35]
	global_load_dword v1, v[2:3], off
.Lrp_skip:
	s_or_b64 exec, exec, s[42:43]
	s_movk_i32 s8, 0x100
	v_cmp_gt_u32_e64 s[50:51], s8, v0
	s_and_saveexec_b64 s[8:9], s[50:51]
	v_mov_b32_e32 v4, 0x21e00
	v_lshl_add_u32 v4, v0, 2, v4
	v_mov_b32_e32 v5, 0
	ds_write_b32 v4, v5
	s_or_b64 exec, exec, s[8:9]
	v_cmp_eq_u32_e32 vcc, 0, v0
	s_and_saveexec_b64 s[8:9], vcc
	v_mov_b32_e32 v4, 0
	v_mov_b32_e32 v5, 0x22c50
	ds_write_b32 v5, v4
	s_or_b64 exec, exec, s[8:9]
	v_and_b32_e32 v18, 63, v0
	v_lshlrev_b32_e32 v4, 3, v18
	global_load_dwordx2 v[12:13], v4, s[44:45] offset:1024
	global_load_dwordx2 v[6:7], v4, s[44:45] offset:1536
	global_load_dwordx2 v[14:15], v4, s[44:45]
	global_load_dwordx2 v[16:17], v4, s[46:47]
	global_load_dwordx2 v[8:9], v4, s[44:45] offset:512
	global_load_dwordx2 v[10:11], v4, s[46:47] offset:512
	s_movk_i32 s48, 0x100
	v_cmp_gt_u32_e32 vcc, s48, v0
	s_and_saveexec_b64 s[48:49], vcc
	s_cbranch_execz .Lskip_wld
	v_lshlrev_b32_e32 v61, 2, v0
	global_load_dword v64, v61, s[44:45]
	global_load_dword v65, v61, s[44:45] offset:1024
	global_load_dword v66, v61, s[46:47]
.Lskip_wld:
	s_or_b64 exec, exec, s[48:49]
	s_movk_i32 s48, 0x1c0
	v_cmp_gt_u32_e32 vcc, s48, v0
	v_mov_b32_e32 v62, 223
	v_mov_b32_e32 v63, 0x24160
	v_cndmask_b32_e32 v62, 0, v62, vcc
	v_lshl_add_u32 v63, v0, 2, v63
	s_movk_i32 s48, 0x1c2
	v_cmp_gt_u32_e32 vcc, s48, v0
	s_and_saveexec_b64 s[48:49], vcc
	ds_write_b32 v63, v62
	s_or_b64 exec, exec, s[48:49]
	s_waitcnt lgkmcnt(0)
	s_sub_i32 s25, s39, s38
	v_mov_b32_e32 v20, s38
	v_or_b32_e32 v23, 0x400, v0
	v_or_b32_e32 v22, 0x800, v0
	v_or_b32_e32 v21, 0xc00, v0
	v_cmp_gt_i32_e32 vcc, s25, v0
	v_cmp_gt_i32_e64 s[6:7], s25, v23
	v_cmp_gt_i32_e64 s[8:9], s25, v22
	v_cndmask_b32_e32 v27, 0, v0, vcc
	v_add_u32_e32 v2, v27, v20
	v_cndmask_b32_e64 v27, 0, v23, s[6:7]
	v_add_u32_e32 v4, v27, v20
	v_cndmask_b32_e64 v27, 0, v22, s[8:9]
	v_add_u32_e32 v24, v27, v20
	v_cmp_gt_i32_e64 s[10:11], s25, v21
	v_ashrrev_i32_e32 v25, 31, v24
	v_ashrrev_i32_e32 v3, 31, v2
	v_cndmask_b32_e64 v27, 0, v21, s[10:11]
	v_lshl_add_u64 v[30:31], v[24:25], 2, s[18:19]
	v_add_u32_e32 v24, v27, v20
	v_lshl_add_u64 v[2:3], v[2:3], 2, s[18:19]
	v_ashrrev_i32_e32 v5, 31, v4
	v_ashrrev_i32_e32 v25, 31, v24
	v_lshl_add_u64 v[4:5], v[4:5], 2, s[18:19]
	v_lshl_add_u64 v[32:33], v[24:25], 2, s[18:19]
	global_load_dword v25, v[2:3], off
	global_load_dword v26, v[4:5], off
	global_load_dword v28, v[30:31], off
	global_load_dword v29, v[32:33], off
	s_and_saveexec_b64 s[42:43], s[40:41]
	s_cbranch_execz .Lrp_skip2
	v_mov_b32_e32 v2, 0x228a0
	v_lshl_add_u32 v2, v0, 2, v2
	s_waitcnt vmcnt(13)
	ds_write_b32 v2, v1
.Lrp_skip2:
	s_or_b64 exec, exec, s[42:43]
	s_waitcnt lgkmcnt(0)
	s_barrier
	v_cmp_gt_i32_e64 s[4:5], s3, v0
	s_and_saveexec_b64 s[12:13], s[4:5]
	s_cbranch_execz .LBB3_8
	v_lshlrev_b32_e32 v1, 2, v0
	v_add_u32_e32 v2, 0x228a0, v1
	ds_read2_b32 v[2:3], v2 offset1:1
	v_add_u32_e32 v1, 0x22580, v1
	s_waitcnt lgkmcnt(0)
	v_sub_u32_e32 v2, v3, v2
	v_add_u32_e32 v2, 3, v2
	v_ashrrev_i32_e32 v2, 2, v2
	ds_write_b32 v1, v2

.Lepi_tail:
	v_sub_u32_e32 v99, v55, v99
	v_cvt_f32_i32_e32 v99, v99
	v_max_f32_e32 v108, 0, v112
	v_max_f32_e32 v109, 0, v113
	v_fma_f32 v100, -v99, v108, v100
	v_fma_f32 v101, -v99, v109, v101
	ds_bpermute_b32 v2, v102, v100
	ds_bpermute_b32 v3, v102, v101
	v_mov_b32_e32 v4, 0x21e00
	v_lshl_add_u32 v4, v56, 2, v4
	s_waitcnt lgkmcnt(0)
	v_add_f32_e32 v100, v100, v2
	v_add_f32_e32 v101, v101, v3
	ds_bpermute_b32 v2, v1, v100
	ds_bpermute_b32 v3, v1, v101
	s_waitcnt lgkmcnt(0)
	v_add_f32_e32 v100, v100, v2
	v_add_f32_e32 v101, v101, v3
	s_and_saveexec_b64 s[8:9], s[66:67]
	s_cbranch_execz .Lepi_done
	s_and_b32 s10, s2, 63
	s_lshl_b32 s10, s10, 10
	v_lshlrev_b32_e32 v4, 2, v56
	v_add_u32_e32 v4, s10, v4
	global_atomic_add_f32 v4, v100, s[74:75]
	global_atomic_add_f32 v4, v101, s[74:75] offset:64
